# P9 norm: 22 bit-trick f32->bf16 RNE packs replaced by v_cvt_pk_bf16_f32 (bit-exact for finite values, same RNE mode)
# speedup vs baseline: 1.0098x; 1.0077x over previous
; #define LAS __attribute__((address_space(3)))
; __device__ __forceinline__ unsigned pk2(float lo, float hi) { return f2bf(lo) | (f2bf(hi) << 16); }
; __device__ __forceinline__ void norm_mod_regs_lds2(const u32x4 (&w)[4], const LAS float* A, const LAS float* B, LAS unsigned char* lrow, int sw, unsigned char* o8row, int lane) {
;     float s = 0.f;
; #pragma unroll
;     for (int j = 0; j < 4; ++j) {
; #pragma unroll
;         for (int i = 0; i < 4; ++i) { const float a = bf_lo(w[j][i]), b = bf_hi(w[j][i]); s += a * a + b * b; } }
;     const float rstd = 1.f / sqrtf(wave_sum(s) * (1.f / DM) + EPS_);
;     const unsigned l8 = (unsigned)lane * 8u;
; #pragma unroll
;     for (int j = 0; j < 4; ++j) {
;         const f32x4 a0 = *(const LAS f32x4*)(A + 512 * j + 8 * lane), a1 = *(const LAS f32x4*)(A + 512 * j + 8 * lane + 4), b0 = *(const LAS f32x4*)(B + 512 * j + 8 * lane), b1 = *(const LAS f32x4*)(B + 512 * j + 8 * lane + 4);
;         const f32x4 h0 = {bf_lo(w[j][0]) * rstd * a0[0] + b0[0], bf_hi(w[j][0]) * rstd * a0[1] + b0[1], bf_lo(w[j][1]) * rstd * a0[2] + b0[2], bf_hi(w[j][1]) * rstd * a0[3] + b0[3]};
;         const f32x4 h1 = {bf_lo(w[j][2]) * rstd * a1[0] + b1[0], bf_hi(w[j][2]) * rstd * a1[1] + b1[1], bf_lo(w[j][3]) * rstd * a1[2] + b1[2], bf_hi(w[j][3]) * rstd * a1[3] + b1[3]};
;         u32x4 o; o.x = pk2(h0[0], h0[1]); o.y = pk2(h0[2], h0[3]); o.z = pk2(h1[0], h1[1]); o.w = pk2(h1[2], h1[3]);
;         *(LAS u32x4*)(lrow + (((lane + 64 * j) ^ sw) << 4)) = o;
;         u32x2 q8; q8.x = pg8::pack4_fp8(h0, pg8::F8_SH); q8.y = pg8::pack4_fp8(h1, pg8::F8_SH); *(u32x2*)((char*)(o8row + 512 * j) + l8) = q8;
.LBB0_1399:
	s_waitcnt vmcnt(7)
	v_and_b32_e32 v233, 0xffff0000, v115
	v_and_b32_e32 v232, 0xffff0000, v114
	v_lshlrev_b32_e32 v231, 16, v115
	v_lshlrev_b32_e32 v230, 16, v114
	v_pk_mul_f32 v[152:153], v[232:233], v[232:233]
	v_and_b32_e32 v237, 0xffff0000, v117
	v_and_b32_e32 v236, 0xffff0000, v116
	v_pk_fma_f32 v[160:161], v[230:231], v[230:231], v[152:153]
	v_lshlrev_b32_e32 v235, 16, v117
	v_lshlrev_b32_e32 v234, 16, v116
	v_pk_mul_f32 v[152:153], v[236:237], v[236:237]
	s_waitcnt vmcnt(6)
	v_and_b32_e32 v241, 0xffff0000, v119
	v_pk_fma_f32 v[214:215], v[234:235], v[234:235], v[152:153]
	v_and_b32_e32 v240, 0xffff0000, v118
	v_add_f32_e32 v160, v160, v161
	v_lshlrev_b32_e32 v239, 16, v119
	v_lshlrev_b32_e32 v238, 16, v118
	v_pk_mul_f32 v[152:153], v[240:241], v[240:241]
	v_add_f32_e32 v160, v214, v160
	v_pk_fma_f32 v[216:217], v[238:239], v[238:239], v[152:153]
	v_and_b32_e32 v245, 0xffff0000, v121
	v_and_b32_e32 v244, 0xffff0000, v120
	v_add_f32_e32 v160, v215, v160
	v_lshlrev_b32_e32 v243, 16, v121
	v_lshlrev_b32_e32 v242, 16, v120
	v_pk_mul_f32 v[152:153], v[244:245], v[244:245]
	v_add_f32_e32 v160, v216, v160
	v_pk_fma_f32 v[218:219], v[242:243], v[242:243], v[152:153]
	s_waitcnt vmcnt(5)
	v_and_b32_e32 v179, 0xffff0000, v123
	v_and_b32_e32 v178, 0xffff0000, v122
	v_add_f32_e32 v160, v217, v160
	v_lshlrev_b32_e32 v181, 16, v123
	v_lshlrev_b32_e32 v180, 16, v122
	v_pk_mul_f32 v[152:153], v[178:179], v[178:179]
	v_add_f32_e32 v160, v218, v160
	v_pk_fma_f32 v[220:221], v[180:181], v[180:181], v[152:153]
	v_and_b32_e32 v157, 0xffff0000, v125
	v_and_b32_e32 v156, 0xffff0000, v124
	v_add_f32_e32 v160, v219, v160
	v_lshlrev_b32_e32 v159, 16, v125
	v_lshlrev_b32_e32 v158, 16, v124
	v_pk_mul_f32 v[152:153], v[156:157], v[156:157]
	v_add_f32_e32 v160, v220, v160
	v_pk_fma_f32 v[222:223], v[158:159], v[158:159], v[152:153]
	s_waitcnt vmcnt(4)
	v_and_b32_e32 v153, 0xffff0000, v127
	v_and_b32_e32 v152, 0xffff0000, v126
	v_add_f32_e32 v160, v221, v160
	v_lshlrev_b32_e32 v155, 16, v127
	v_lshlrev_b32_e32 v154, 16, v126
	v_pk_mul_f32 v[224:225], v[152:153], v[152:153]
	v_add_f32_e32 v160, v222, v160
	v_and_b32_e32 v147, 0xffff0000, v129
	v_and_b32_e32 v146, 0xffff0000, v128
	v_pk_fma_f32 v[224:225], v[154:155], v[154:155], v[224:225]
	v_add_f32_e32 v160, v223, v160
	v_lshlrev_b32_e32 v149, 16, v129
	v_lshlrev_b32_e32 v148, 16, v128
	v_pk_mul_f32 v[150:151], v[146:147], v[146:147]
	v_add_f32_e32 v160, v224, v160
	v_pk_fma_f32 v[150:151], v[148:149], v[148:149], v[150:151]
	v_add_f32_e32 v160, v225, v160
	v_add_f32_e32 v150, v150, v160
	v_add_f32_e32 v150, v151, v150
	ds_bpermute_b32 v151, v183, v150
	s_add_i32 s24, s40, s27
	s_ashr_i32 s25, s24, 31
	s_lshl_b64 s[22:23], s[24:25], 11
	ds_read_b128 v[214:217], v189
	ds_read_b128 v[218:221], v189 offset:16
	s_waitcnt lgkmcnt(2)
	v_add_f32_e32 v150, v150, v151
	ds_bpermute_b32 v151, v184, v150
	ds_read_b128 v[222:225], v190
	ds_read_b128 v[226:229], v190 offset:16
	s_waitcnt lgkmcnt(4)
	v_mov_b32_e32 v246, v214
	s_waitcnt lgkmcnt(3)
	v_mov_b32_e32 v214, v218
	v_mov_b32_e32 v247, v216
	s_waitcnt lgkmcnt(2)
	v_add_f32_e32 v150, v150, v151
	ds_bpermute_b32 v151, v185, v150
	v_mov_b32_e32 v216, v215
	v_mov_b32_e32 v215, v220
	v_mov_b32_e32 v220, v219
	s_waitcnt lgkmcnt(2)
	v_mov_b32_e32 v248, v222
	s_waitcnt lgkmcnt(0)
	v_add_f32_e32 v160, v150, v151
	ds_bpermute_b32 v161, v186, v160
	v_lshl_add_u64 v[150:151], v[176:177], 0, s[22:23]
	v_mov_b32_e32 v249, v224
	v_mov_b32_e32 v224, v223
	v_mov_b32_e32 v222, v226
	s_waitcnt lgkmcnt(0)
	v_add_f32_e32 v160, v160, v161
	ds_bpermute_b32 v161, v187, v160
	v_mov_b32_e32 v223, v228
	v_mov_b32_e32 v228, v227
	s_waitcnt lgkmcnt(0)
	v_add_f32_e32 v160, v160, v161
	ds_bpermute_b32 v161, v188, v160
	s_waitcnt lgkmcnt(0)
	v_add_f32_e32 v160, v160, v161
	v_fmamk_f32 v160, v160, 0x3a000000, v195
	v_mul_f32_e32 v161, 0x4f800000, v160
	v_cmp_gt_f32_e32 vcc, s53, v160
	s_nop 1
	v_cndmask_b32_e32 v160, v160, v161, vcc
	v_sqrt_f32_e32 v161, v160
	s_nop 0
	v_add_u32_e32 v164, -1, v161
	v_fma_f32 v213, -v164, v161, v160
	v_cmp_ge_f32_e64 s[22:23], 0, v213
	v_add_u32_e32 v213, 1, v161
	s_nop 0
	v_cndmask_b32_e64 v164, v161, v164, s[22:23]
	v_fma_f32 v161, -v213, v161, v160
	v_cmp_lt_f32_e64 s[22:23], 0, v161
	s_nop 1
	v_cndmask_b32_e64 v161, v164, v213, s[22:23]
	v_mul_f32_e32 v164, 0x37800000, v161
	v_cndmask_b32_e32 v161, v161, v164, vcc
	v_cmp_class_f32_e32 vcc, v160, v196
	s_nop 1
	v_cndmask_b32_e32 v160, v161, v160, vcc
	v_div_scale_f32 v161, s[22:23], v160, v160, 1.0
	v_rcp_f32_e32 v164, v161
	s_nop 0
	v_fma_f32 v213, -v161, v164, 1.0
	v_fmac_f32_e32 v164, v213, v164
	v_div_scale_f32 v213, vcc, 1.0, v160, 1.0
	v_mul_f32_e32 v218, v213, v164
	v_fma_f32 v219, -v161, v218, v213
	v_fmac_f32_e32 v218, v219, v164
	v_fma_f32 v161, -v161, v218, v213
	v_div_fmas_f32 v161, v161, v164, v218
	v_div_fixup_f32 v160, v161, v160, 1.0
	v_pk_mul_f32 v[226:227], v[160:161], v[232:233] op_sel_hi:[0,1]
	v_pk_fma_f32 v[224:225], v[216:217], v[226:227], v[224:225]
	v_pk_mul_f32 v[216:217], v[160:161], v[234:235] op_sel_hi:[0,1]
	v_pk_mul_f32 v[218:219], v[160:161], v[230:231] op_sel_hi:[0,1]
	v_pk_fma_f32 v[214:215], v[214:215], v[216:217], v[222:223]
	v_pk_mul_f32 v[216:217], v[160:161], v[236:237] op_sel_hi:[0,1]
	v_pk_fma_f32 v[218:219], v[246:247], v[218:219], v[248:249]
	v_pk_fma_f32 v[220:221], v[220:221], v[216:217], v[228:229]
	v_bfe_u32 v216, v224, 16, 1
	v_add3_u32 v222, v224, v216, s54
	v_bfe_u32 v216, v218, 16, 1
	v_bfe_u32 v217, v219, 16, 1
	v_add3_u32 v217, v219, v217, s54
	v_add3_u32 v216, v218, v216, s54
	v_lshrrev_b32_e32 v227, 16, v216
	v_lshrrev_b32_e32 v228, 16, v217
	v_cvt_pk_bf16_f32 v217, v215, v221
	v_cvt_pk_bf16_f32 v216, v214, v220
	v_med3_f32 v161, v218, s55, v210
	v_med3_f32 v164, v224, s55, v210
	v_mov_b32_e32 v218, 0
	v_cvt_pk_fp8_f32 v218, v161, v164
	v_med3_f32 v161, v219, s55, v210
	v_med3_f32 v214, v214, s55, v210
	v_med3_f32 v220, v220, s55, v210
	v_mov_b32_e32 v219, 0
	v_cvt_pk_fp8_f32 v219, v214, v220
	v_med3_f32 v164, v225, s55, v210
	v_cvt_pk_fp8_f32 v218, v161, v164 op_sel:[0,0,1]
	v_med3_f32 v161, v215, s55, v210
	v_med3_f32 v164, v221, s55, v210
	v_cvt_pk_fp8_f32 v219, v161, v164 op_sel:[0,0,1]
	v_bfe_u32 v213, v225, 16, 1
	v_add3_u32 v213, v225, v213, s54
	v_and_or_b32 v215, v213, s52, v228
	v_and_or_b32 v214, v222, s52, v227
	ds_write_b128 v197, v[214:217]
	global_store_dwordx2 v[150:151], v[218:219], off
	ds_read_b128 v[214:217], v189 offset:2048
	ds_read_b128 v[218:221], v189 offset:2064
	ds_read_b128 v[222:225], v190 offset:2048
	ds_read_b128 v[226:229], v190 offset:2064
	v_pk_mul_f32 v[230:231], v[160:161], v[238:239] op_sel_hi:[0,1]
	s_waitcnt lgkmcnt(3)
; #define LAS __attribute__((address_space(3)))
; __device__ __forceinline__ unsigned pk2(float lo, float hi) { return f2bf(lo) | (f2bf(hi) << 16); }
; __device__ __forceinline__ void norm_mod_regs_lds2(const u32x4 (&w)[4], const LAS float* A, const LAS float* B, LAS unsigned char* lrow, int sw, unsigned char* o8row, int lane) {
;     ...
;     for (int j = 0; j < 4; ++j) {
;         const f32x4 a0 = *(const LAS f32x4*)(A + 512 * j + 8 * lane), a1 = *(const LAS f32x4*)(A + 512 * j + 8 * lane + 4), b0 = *(const LAS f32x4*)(B + 512 * j + 8 * lane), b1 = *(const LAS f32x4*)(B + 512 * j + 8 * lane + 4);
;         const f32x4 h0 = {bf_lo(w[j][0]) * rstd * a0[0] + b0[0], bf_hi(w[j][0]) * rstd * a0[1] + b0[1], bf_lo(w[j][1]) * rstd * a0[2] + b0[2], bf_hi(w[j][1]) * rstd * a0[3] + b0[3]};
;         const f32x4 h1 = {bf_lo(w[j][2]) * rstd * a1[0] + b1[0], bf_hi(w[j][2]) * rstd * a1[1] + b1[1], bf_lo(w[j][3]) * rstd * a1[2] + b1[2], bf_hi(w[j][3]) * rstd * a1[3] + b1[3]};
;         u32x4 o; o.x = pk2(h0[0], h0[1]); o.y = pk2(h0[2], h0[3]); o.z = pk2(h1[0], h1[1]); o.w = pk2(h1[2], h1[3]);
;         *(LAS u32x4*)(lrow + (((lane + 64 * j) ^ sw) << 4)) = o;
;         u32x2 q8; q8.x = pg8::pack4_fp8(h0, pg8::F8_SH); q8.y = pg8::pack4_fp8(h1, pg8::F8_SH); *(u32x2*)((char*)(o8row + 512 * j) + l8) = q8;
	v_mov_b32_e32 v232, v214
	v_mov_b32_e32 v233, v216
	s_waitcnt lgkmcnt(1)
	v_mov_b32_e32 v234, v222
	v_mov_b32_e32 v235, v224
	v_pk_fma_f32 v[230:231], v[232:233], v[230:231], v[234:235]
	v_pk_mul_f32 v[232:233], v[160:161], v[240:241] op_sel_hi:[0,1]
	v_mov_b32_e32 v216, v215
	v_mov_b32_e32 v224, v223
	v_pk_fma_f32 v[214:215], v[216:217], v[232:233], v[224:225]
	v_pk_mul_f32 v[216:217], v[160:161], v[242:243] op_sel_hi:[0,1]
	v_mov_b32_e32 v222, v218
	v_mov_b32_e32 v223, v220
	s_waitcnt lgkmcnt(0)
	v_mov_b32_e32 v224, v226
	v_mov_b32_e32 v225, v228
	v_pk_fma_f32 v[222:223], v[222:223], v[216:217], v[224:225]
	v_pk_mul_f32 v[216:217], v[160:161], v[244:245] op_sel_hi:[0,1]
	v_mov_b32_e32 v220, v219
	v_mov_b32_e32 v228, v227
	v_pk_fma_f32 v[218:219], v[220:221], v[216:217], v[228:229]
	v_bfe_u32 v216, v214, 16, 1
	v_add3_u32 v224, v214, v216, s54
	v_bfe_u32 v216, v230, 16, 1
	v_add3_u32 v216, v230, v216, s54
	v_lshrrev_b32_e32 v225, 16, v216
	v_cvt_pk_bf16_f32 v217, v223, v219
	v_cvt_pk_bf16_f32 v216, v222, v218
	v_med3_f32 v161, v230, s55, v210
	v_med3_f32 v164, v214, s55, v210
	v_mov_b32_e32 v220, 0
	v_cvt_pk_bf16_f32 v213, v231, v215
	v_cvt_pk_fp8_f32 v220, v161, v164
	v_med3_f32 v164, v215, s55, v210
	v_med3_f32 v214, v222, s55, v210
	v_med3_f32 v215, v218, s55, v210
	v_mov_b32_e32 v221, 0
	v_cvt_pk_fp8_f32 v221, v214, v215
	v_med3_f32 v161, v231, s55, v210
	v_cvt_pk_fp8_f32 v220, v161, v164 op_sel:[0,0,1]
	v_med3_f32 v161, v223, s55, v210
	v_med3_f32 v164, v219, s55, v210
	v_cvt_pk_fp8_f32 v221, v161, v164 op_sel:[0,0,1]
	v_mov_b32_e32 v215, v213
	v_and_or_b32 v214, v224, s52, v225
	ds_write_b128 v198, v[214:217]
	global_store_dwordx2 v[150:151], v[220:221], off offset:512
	ds_read_b128 v[214:217], v189 offset:4096
	ds_read_b128 v[218:221], v189 offset:4112
	ds_read_b128 v[222:225], v190 offset:4096
	ds_read_b128 v[226:229], v190 offset:4112
	v_pk_mul_f32 v[178:179], v[160:161], v[178:179] op_sel_hi:[0,1]
	s_waitcnt lgkmcnt(3)
	v_mov_b32_e32 v231, v216
	v_mov_b32_e32 v216, v215
	s_waitcnt lgkmcnt(1)
	v_mov_b32_e32 v233, v224
	v_mov_b32_e32 v224, v223
	v_pk_fma_f32 v[178:179], v[178:179], v[216:217], v[224:225]
	v_mov_b32_e32 v215, v220
	s_waitcnt lgkmcnt(0)
	v_mov_b32_e32 v217, v228
	v_pk_mul_f32 v[156:157], v[160:161], v[156:157] op_sel_hi:[0,1]
	v_mov_b32_e32 v220, v219
	v_mov_b32_e32 v228, v227
	v_pk_mul_f32 v[180:181], v[160:161], v[180:181] op_sel_hi:[0,1]
	v_mov_b32_e32 v230, v214
	v_mov_b32_e32 v232, v222
	v_pk_mul_f32 v[158:159], v[160:161], v[158:159] op_sel_hi:[0,1]
	v_mov_b32_e32 v214, v218
	v_mov_b32_e32 v216, v226
	v_pk_fma_f32 v[156:157], v[156:157], v[220:221], v[228:229]
	v_pk_fma_f32 v[180:181], v[180:181], v[230:231], v[232:233]
	v_pk_fma_f32 v[214:215], v[158:159], v[214:215], v[216:217]
	v_bfe_u32 v161, v179, 16, 1
	v_cvt_pk_bf16_f32 v164, v180, v178
	v_bfe_u32 v216, v181, 16, 1
	v_cvt_pk_bf16_f32 v159, v215, v157
	v_cvt_pk_bf16_f32 v158, v214, v156
	v_med3_f32 v180, v180, s55, v210
	v_med3_f32 v213, v178, s55, v210
	v_mov_b32_e32 v178, 0
	v_add3_u32 v161, v179, v161, s54
	v_add3_u32 v216, v181, v216, s54
	v_cvt_pk_fp8_f32 v178, v180, v213
	v_med3_f32 v180, v181, s55, v210
	v_med3_f32 v181, v179, s55, v210
	v_med3_f32 v213, v214, s55, v210
	v_med3_f32 v156, v156, s55, v210
	v_mov_b32_e32 v179, 0
	v_cvt_pk_fp8_f32 v179, v213, v156
	v_med3_f32 v156, v215, s55, v210
	v_med3_f32 v157, v157, s55, v210
	v_cvt_pk_fp8_f32 v178, v180, v181 op_sel:[0,0,1]
	v_cvt_pk_fp8_f32 v179, v156, v157 op_sel:[0,0,1]
	v_lshrrev_b32_e32 v216, 16, v216
	v_and_or_b32 v157, v161, s52, v216
	v_mov_b32_e32 v156, v164
	ds_write_b128 v199, v[156:159]
	global_store_dwordx2 v[150:151], v[178:179], off offset:1024
	ds_read_b128 v[156:159], v189 offset:6144
	ds_read_b128 v[178:181], v189 offset:6160
	ds_read_b128 v[214:217], v190 offset:6144
	ds_read_b128 v[218:221], v190 offset:6160
	v_pk_mul_f32 v[152:153], v[160:161], v[152:153] op_sel_hi:[0,1]
	s_waitcnt lgkmcnt(3)
	v_mov_b32_e32 v223, v158
	v_mov_b32_e32 v158, v157
	s_waitcnt lgkmcnt(1)
	v_mov_b32_e32 v225, v216
	v_mov_b32_e32 v216, v215
	v_pk_fma_f32 v[152:153], v[152:153], v[158:159], v[216:217]
	v_mov_b32_e32 v157, v180
	s_waitcnt lgkmcnt(0)
	v_mov_b32_e32 v159, v220
	v_pk_mul_f32 v[146:147], v[160:161], v[146:147] op_sel_hi:[0,1]
	v_mov_b32_e32 v180, v179
	v_mov_b32_e32 v220, v219
	v_pk_mul_f32 v[154:155], v[160:161], v[154:155] op_sel_hi:[0,1]
	v_mov_b32_e32 v222, v156
	v_mov_b32_e32 v224, v214
	v_pk_mul_f32 v[148:149], v[160:161], v[148:149] op_sel_hi:[0,1]
	v_mov_b32_e32 v156, v178
	v_mov_b32_e32 v158, v218
	v_pk_fma_f32 v[146:147], v[146:147], v[180:181], v[220:221]
	v_pk_fma_f32 v[154:155], v[154:155], v[222:223], v[224:225]
	v_pk_fma_f32 v[156:157], v[148:149], v[156:157], v[158:159]
	v_bfe_u32 v158, v153, 16, 1
	v_cvt_pk_bf16_f32 v159, v154, v152
	v_bfe_u32 v161, v155, 16, 1
	v_cvt_pk_bf16_f32 v149, v157, v147
	v_cvt_pk_bf16_f32 v148, v156, v146
	v_med3_f32 v154, v154, s55, v210
	v_med3_f32 v160, v152, s55, v210
	v_mov_b32_e32 v152, 0
	v_add3_u32 v158, v153, v158, s54
	v_add3_u32 v161, v155, v161, s54
	v_cvt_pk_fp8_f32 v152, v154, v160
	v_med3_f32 v154, v155, s55, v210
	v_med3_f32 v155, v153, s55, v210
	v_med3_f32 v156, v156, s55, v210
	v_med3_f32 v146, v146, s55, v210
	v_mov_b32_e32 v153, 0
	v_cvt_pk_fp8_f32 v153, v156, v146
	v_med3_f32 v146, v157, s55, v210
	v_med3_f32 v147, v147, s55, v210
	v_cvt_pk_fp8_f32 v152, v154, v155 op_sel:[0,0,1]
	v_cvt_pk_fp8_f32 v153, v146, v147 op_sel:[0,0,1]
	v_lshrrev_b32_e32 v161, 16, v161
	v_and_or_b32 v147, v158, s52, v161
	v_mov_b32_e32 v146, v159
	ds_write_b128 v200, v[146:149]
	global_store_dwordx2 v[150:151], v[152:153], off offset:1536
	s_waitcnt vmcnt(7)
; #define LAS __attribute__((address_space(3)))
; __device__ __forceinline__ unsigned pk2(float lo, float hi) { return f2bf(lo) | (f2bf(hi) << 16); }
; __device__ __forceinline__ void norm_mod_regs_lds2(const u32x4 (&w)[4], const LAS float* A, const LAS float* B, LAS unsigned char* lrow, int sw, unsigned char* o8row, int lane) {
;     float s = 0.f;
; #pragma unroll
;     for (int j = 0; j < 4; ++j) {
; #pragma unroll
;         for (int i = 0; i < 4; ++i) { const float a = bf_lo(w[j][i]), b = bf_hi(w[j][i]); s += a * a + b * b; } }
;     const float rstd = 1.f / sqrtf(wave_sum(s) * (1.f / DM) + EPS_);
;     const unsigned l8 = (unsigned)lane * 8u;
; #pragma unroll
;     for (int j = 0; j < 4; ++j) {
;         const f32x4 a0 = *(const LAS f32x4*)(A + 512 * j + 8 * lane), a1 = *(const LAS f32x4*)(A + 512 * j + 8 * lane + 4), b0 = *(const LAS f32x4*)(B + 512 * j + 8 * lane), b1 = *(const LAS f32x4*)(B + 512 * j + 8 * lane + 4);
;         const f32x4 h0 = {bf_lo(w[j][0]) * rstd * a0[0] + b0[0], bf_hi(w[j][0]) * rstd * a0[1] + b0[1], bf_lo(w[j][1]) * rstd * a0[2] + b0[2], bf_hi(w[j][1]) * rstd * a0[3] + b0[3]};
;         const f32x4 h1 = {bf_lo(w[j][2]) * rstd * a1[0] + b1[0], bf_hi(w[j][2]) * rstd * a1[1] + b1[1], bf_lo(w[j][3]) * rstd * a1[2] + b1[2], bf_hi(w[j][3]) * rstd * a1[3] + b1[3]};
;         u32x4 o; o.x = pk2(h0[0], h0[1]); o.y = pk2(h0[2], h0[3]); o.z = pk2(h1[0], h1[1]); o.w = pk2(h1[2], h1[3]);
;         *(LAS u32x4*)(lrow + (((lane + 64 * j) ^ sw) << 4)) = o;
;         u32x2 q8; q8.x = pg8::pack4_fp8(h0, pg8::F8_SH); q8.y = pg8::pack4_fp8(h1, pg8::F8_SH); *(u32x2*)((char*)(o8row + 512 * j) + l8) = q8;
	v_and_b32_e32 v233, 0xffff0000, v131
	v_and_b32_e32 v232, 0xffff0000, v130
	v_lshlrev_b32_e32 v231, 16, v131
	v_lshlrev_b32_e32 v230, 16, v130
	v_pk_mul_f32 v[152:153], v[232:233], v[232:233]
	v_and_b32_e32 v237, 0xffff0000, v133
	v_and_b32_e32 v236, 0xffff0000, v132
	v_pk_fma_f32 v[160:161], v[230:231], v[230:231], v[152:153]
	v_lshlrev_b32_e32 v235, 16, v133
	v_lshlrev_b32_e32 v234, 16, v132
	v_pk_mul_f32 v[152:153], v[236:237], v[236:237]
	s_waitcnt vmcnt(6)
	v_and_b32_e32 v241, 0xffff0000, v135
	v_pk_fma_f32 v[214:215], v[234:235], v[234:235], v[152:153]
	v_and_b32_e32 v240, 0xffff0000, v134
	v_add_f32_e32 v160, v160, v161
	v_lshlrev_b32_e32 v239, 16, v135
	v_lshlrev_b32_e32 v238, 16, v134
	v_pk_mul_f32 v[152:153], v[240:241], v[240:241]
	v_add_f32_e32 v160, v214, v160
	v_pk_fma_f32 v[216:217], v[238:239], v[238:239], v[152:153]
	v_and_b32_e32 v245, 0xffff0000, v137
	v_and_b32_e32 v244, 0xffff0000, v136
	v_add_f32_e32 v160, v215, v160
	v_lshlrev_b32_e32 v243, 16, v137
	v_lshlrev_b32_e32 v242, 16, v136
	v_pk_mul_f32 v[152:153], v[244:245], v[244:245]
	v_add_f32_e32 v160, v216, v160
	v_pk_fma_f32 v[218:219], v[242:243], v[242:243], v[152:153]
	s_waitcnt vmcnt(5)
	v_and_b32_e32 v179, 0xffff0000, v139
	v_and_b32_e32 v178, 0xffff0000, v138
	v_add_f32_e32 v160, v217, v160
	v_lshlrev_b32_e32 v181, 16, v139
	v_lshlrev_b32_e32 v180, 16, v138
	v_pk_mul_f32 v[152:153], v[178:179], v[178:179]
	v_add_f32_e32 v160, v218, v160
	v_pk_fma_f32 v[220:221], v[180:181], v[180:181], v[152:153]
	v_and_b32_e32 v157, 0xffff0000, v141
	v_and_b32_e32 v156, 0xffff0000, v140
	v_add_f32_e32 v160, v219, v160
	v_lshlrev_b32_e32 v159, 16, v141
	v_lshlrev_b32_e32 v158, 16, v140
	v_pk_mul_f32 v[152:153], v[156:157], v[156:157]
	v_add_f32_e32 v160, v220, v160
	v_pk_fma_f32 v[222:223], v[158:159], v[158:159], v[152:153]
	s_waitcnt vmcnt(4)
	v_and_b32_e32 v153, 0xffff0000, v143
	v_and_b32_e32 v152, 0xffff0000, v142
	v_add_f32_e32 v160, v221, v160
	v_lshlrev_b32_e32 v155, 16, v143
	v_lshlrev_b32_e32 v154, 16, v142
	v_pk_mul_f32 v[224:225], v[152:153], v[152:153]
	v_add_f32_e32 v160, v222, v160
	v_and_b32_e32 v147, 0xffff0000, v145
	v_and_b32_e32 v146, 0xffff0000, v144
	v_pk_fma_f32 v[224:225], v[154:155], v[154:155], v[224:225]
	v_add_f32_e32 v160, v223, v160
	v_lshlrev_b32_e32 v149, 16, v145
	v_lshlrev_b32_e32 v148, 16, v144
	v_pk_mul_f32 v[150:151], v[146:147], v[146:147]
	v_add_f32_e32 v160, v224, v160
	v_pk_fma_f32 v[150:151], v[148:149], v[148:149], v[150:151]
	v_add_f32_e32 v160, v225, v160
	v_add_f32_e32 v150, v150, v160
	v_add_f32_e32 v150, v151, v150
	ds_bpermute_b32 v151, v183, v150
	s_add_i32 s50, s24, 1
	s_ashr_i32 s51, s50, 31
	s_lshl_b64 s[22:23], s[50:51], 11
	ds_read_b128 v[214:217], v189
	ds_read_b128 v[218:221], v189 offset:16
	s_waitcnt lgkmcnt(2)
	v_add_f32_e32 v150, v150, v151
	ds_bpermute_b32 v151, v184, v150
	ds_read_b128 v[222:225], v190
	ds_read_b128 v[226:229], v190 offset:16
	s_waitcnt lgkmcnt(4)
	v_mov_b32_e32 v246, v214
	s_waitcnt lgkmcnt(3)
	v_mov_b32_e32 v214, v218
	v_mov_b32_e32 v247, v216
	s_waitcnt lgkmcnt(2)
	v_add_f32_e32 v150, v150, v151
	ds_bpermute_b32 v151, v185, v150
	v_mov_b32_e32 v216, v215
	v_mov_b32_e32 v215, v220
	v_mov_b32_e32 v220, v219
	s_waitcnt lgkmcnt(2)
	v_mov_b32_e32 v248, v222
	s_waitcnt lgkmcnt(0)
	v_add_f32_e32 v160, v150, v151
	ds_bpermute_b32 v161, v186, v160
	v_lshl_add_u64 v[150:151], v[176:177], 0, s[22:23]
	v_mov_b32_e32 v249, v224
	v_mov_b32_e32 v224, v223
	v_mov_b32_e32 v222, v226
	s_waitcnt lgkmcnt(0)
	v_add_f32_e32 v160, v160, v161
	ds_bpermute_b32 v161, v187, v160
	v_mov_b32_e32 v223, v228
	v_mov_b32_e32 v228, v227
	s_waitcnt lgkmcnt(0)
	v_add_f32_e32 v160, v160, v161
	ds_bpermute_b32 v161, v188, v160
	s_waitcnt lgkmcnt(0)
	v_add_f32_e32 v160, v160, v161
	v_fmamk_f32 v160, v160, 0x3a000000, v195
	v_mul_f32_e32 v161, 0x4f800000, v160
	v_cmp_gt_f32_e32 vcc, s53, v160
	s_nop 1
	v_cndmask_b32_e32 v160, v160, v161, vcc
	v_sqrt_f32_e32 v161, v160
	s_nop 0
	v_add_u32_e32 v164, -1, v161
	v_fma_f32 v213, -v164, v161, v160
	v_cmp_ge_f32_e64 s[22:23], 0, v213
	v_add_u32_e32 v213, 1, v161
	s_nop 0
	v_cndmask_b32_e64 v164, v161, v164, s[22:23]
	v_fma_f32 v161, -v213, v161, v160
	v_cmp_lt_f32_e64 s[22:23], 0, v161
	s_nop 1
	v_cndmask_b32_e64 v161, v164, v213, s[22:23]
	v_mul_f32_e32 v164, 0x37800000, v161
	v_cndmask_b32_e32 v161, v161, v164, vcc
	v_cmp_class_f32_e32 vcc, v160, v196
	s_nop 1
	v_cndmask_b32_e32 v160, v161, v160, vcc
	v_div_scale_f32 v161, s[22:23], v160, v160, 1.0
	v_rcp_f32_e32 v164, v161
	s_nop 0
	v_fma_f32 v213, -v161, v164, 1.0
	v_fmac_f32_e32 v164, v213, v164
	v_div_scale_f32 v213, vcc, 1.0, v160, 1.0
	v_mul_f32_e32 v218, v213, v164
	v_fma_f32 v219, -v161, v218, v213
	v_fmac_f32_e32 v218, v219, v164
	v_fma_f32 v161, -v161, v218, v213
	v_div_fmas_f32 v161, v161, v164, v218
	v_div_fixup_f32 v160, v161, v160, 1.0
	v_pk_mul_f32 v[226:227], v[160:161], v[232:233] op_sel_hi:[0,1]
	v_pk_fma_f32 v[224:225], v[216:217], v[226:227], v[224:225]
	v_pk_mul_f32 v[216:217], v[160:161], v[234:235] op_sel_hi:[0,1]
	v_pk_mul_f32 v[218:219], v[160:161], v[230:231] op_sel_hi:[0,1]
	v_pk_fma_f32 v[214:215], v[214:215], v[216:217], v[222:223]
	v_pk_mul_f32 v[216:217], v[160:161], v[236:237] op_sel_hi:[0,1]
	v_pk_fma_f32 v[218:219], v[246:247], v[218:219], v[248:249]
	v_pk_fma_f32 v[220:221], v[220:221], v[216:217], v[228:229]
	v_bfe_u32 v216, v224, 16, 1
	v_add3_u32 v222, v224, v216, s54
	v_bfe_u32 v216, v218, 16, 1
	v_bfe_u32 v217, v219, 16, 1
	v_add3_u32 v217, v219, v217, s54
	v_add3_u32 v216, v218, v216, s54
	v_lshrrev_b32_e32 v227, 16, v216
	v_lshrrev_b32_e32 v228, 16, v217
	v_cvt_pk_bf16_f32 v217, v215, v221
	v_cvt_pk_bf16_f32 v216, v214, v220
	v_med3_f32 v161, v218, s55, v210
	v_med3_f32 v164, v224, s55, v210
	v_mov_b32_e32 v218, 0
	v_cvt_pk_fp8_f32 v218, v161, v164
	v_med3_f32 v161, v219, s55, v210
	v_med3_f32 v214, v214, s55, v210
	v_med3_f32 v220, v220, s55, v210
	v_mov_b32_e32 v219, 0
	v_cvt_pk_fp8_f32 v219, v214, v220
	v_med3_f32 v164, v225, s55, v210
	v_cvt_pk_fp8_f32 v218, v161, v164 op_sel:[0,0,1]
	v_med3_f32 v161, v215, s55, v210
	v_med3_f32 v164, v221, s55, v210
	v_cvt_pk_fp8_f32 v219, v161, v164 op_sel:[0,0,1]
	v_bfe_u32 v213, v225, 16, 1
	v_add3_u32 v213, v225, v213, s54
	v_and_or_b32 v215, v213, s52, v228
	v_and_or_b32 v214, v222, s52, v227
	ds_write_b128 v201, v[214:217]
	global_store_dwordx2 v[150:151], v[218:219], off
	ds_read_b128 v[214:217], v189 offset:2048
	ds_read_b128 v[218:221], v189 offset:2064
	ds_read_b128 v[222:225], v190 offset:2048
	ds_read_b128 v[226:229], v190 offset:2064
	v_pk_mul_f32 v[230:231], v[160:161], v[238:239] op_sel_hi:[0,1]
	s_waitcnt lgkmcnt(3)
; #define LAS __attribute__((address_space(3)))
; __device__ __forceinline__ unsigned pk2(float lo, float hi) { return f2bf(lo) | (f2bf(hi) << 16); }
; __device__ __forceinline__ void norm_mod_regs_lds2(const u32x4 (&w)[4], const LAS float* A, const LAS float* B, LAS unsigned char* lrow, int sw, unsigned char* o8row, int lane) {
;     ...
;     for (int j = 0; j < 4; ++j) {
;         const f32x4 a0 = *(const LAS f32x4*)(A + 512 * j + 8 * lane), a1 = *(const LAS f32x4*)(A + 512 * j + 8 * lane + 4), b0 = *(const LAS f32x4*)(B + 512 * j + 8 * lane), b1 = *(const LAS f32x4*)(B + 512 * j + 8 * lane + 4);
;         const f32x4 h0 = {bf_lo(w[j][0]) * rstd * a0[0] + b0[0], bf_hi(w[j][0]) * rstd * a0[1] + b0[1], bf_lo(w[j][1]) * rstd * a0[2] + b0[2], bf_hi(w[j][1]) * rstd * a0[3] + b0[3]};
;         const f32x4 h1 = {bf_lo(w[j][2]) * rstd * a1[0] + b1[0], bf_hi(w[j][2]) * rstd * a1[1] + b1[1], bf_lo(w[j][3]) * rstd * a1[2] + b1[2], bf_hi(w[j][3]) * rstd * a1[3] + b1[3]};
;         u32x4 o; o.x = pk2(h0[0], h0[1]); o.y = pk2(h0[2], h0[3]); o.z = pk2(h1[0], h1[1]); o.w = pk2(h1[2], h1[3]);
;         *(LAS u32x4*)(lrow + (((lane + 64 * j) ^ sw) << 4)) = o;
;         u32x2 q8; q8.x = pg8::pack4_fp8(h0, pg8::F8_SH); q8.y = pg8::pack4_fp8(h1, pg8::F8_SH); *(u32x2*)((char*)(o8row + 512 * j) + l8) = q8;
; __device__ __forceinline__ void p9_fused4(Frame& F) {
;     ...
; #pragma unroll
;         for (int i = NFR; i < 32; ++i) fbr[i] = *(const bf16x8*)(wrb + (size_t)(i >> 2) * 4096 + (lo16 + (unsigned)((i & 3) * 1024)));
;         if (pass < 3) {
; #pragma unroll
;             for (int q = 0; q < 2; ++q)
; #pragma unroll
;                 for (int j = 0; j < 4; ++j) xw[q][j] = ldu16(WSP(bf16_t, WS_X1) + (size_t)(t0 + (pass + 1) * 16 + wave * 2 + q) * DM + 512 * j, lo16);
	v_mov_b32_e32 v232, v214
	v_mov_b32_e32 v233, v216
	s_waitcnt lgkmcnt(1)
	v_mov_b32_e32 v234, v222
	v_mov_b32_e32 v235, v224
	v_pk_fma_f32 v[230:231], v[230:231], v[232:233], v[234:235]
	v_pk_mul_f32 v[232:233], v[160:161], v[240:241] op_sel_hi:[0,1]
	v_mov_b32_e32 v216, v215
	v_mov_b32_e32 v224, v223
	v_pk_fma_f32 v[214:215], v[232:233], v[216:217], v[224:225]
	v_pk_mul_f32 v[216:217], v[160:161], v[242:243] op_sel_hi:[0,1]
	v_mov_b32_e32 v222, v218
	v_mov_b32_e32 v223, v220
	s_waitcnt lgkmcnt(0)
	v_mov_b32_e32 v224, v226
	v_mov_b32_e32 v225, v228
	v_pk_fma_f32 v[222:223], v[216:217], v[222:223], v[224:225]
	v_pk_mul_f32 v[216:217], v[160:161], v[244:245] op_sel_hi:[0,1]
	v_mov_b32_e32 v220, v219
	v_mov_b32_e32 v228, v227
	v_pk_fma_f32 v[218:219], v[216:217], v[220:221], v[228:229]
	v_bfe_u32 v216, v214, 16, 1
	v_add3_u32 v224, v214, v216, s54
	v_bfe_u32 v216, v230, 16, 1
	v_add3_u32 v216, v230, v216, s54
	v_lshrrev_b32_e32 v225, 16, v216
	v_cvt_pk_bf16_f32 v217, v223, v219
	v_cvt_pk_bf16_f32 v216, v222, v218
	v_med3_f32 v161, v230, s55, v210
	v_med3_f32 v164, v214, s55, v210
	v_mov_b32_e32 v220, 0
	v_cvt_pk_bf16_f32 v213, v231, v215
	v_cvt_pk_fp8_f32 v220, v161, v164
	v_med3_f32 v164, v215, s55, v210
	v_med3_f32 v214, v222, s55, v210
	v_med3_f32 v215, v218, s55, v210
	v_mov_b32_e32 v221, 0
	v_cvt_pk_fp8_f32 v221, v214, v215
	v_med3_f32 v161, v231, s55, v210
	v_cvt_pk_fp8_f32 v220, v161, v164 op_sel:[0,0,1]
	v_med3_f32 v161, v223, s55, v210
	v_med3_f32 v164, v219, s55, v210
	v_cvt_pk_fp8_f32 v221, v161, v164 op_sel:[0,0,1]
	v_mov_b32_e32 v215, v213
	v_and_or_b32 v214, v224, s52, v225
	ds_write_b128 v202, v[214:217]
	global_store_dwordx2 v[150:151], v[220:221], off offset:512
	ds_read_b128 v[214:217], v189 offset:4096
	ds_read_b128 v[218:221], v189 offset:4112
	ds_read_b128 v[222:225], v190 offset:4096
	ds_read_b128 v[226:229], v190 offset:4112
	v_pk_mul_f32 v[178:179], v[160:161], v[178:179] op_sel_hi:[0,1]
	s_waitcnt lgkmcnt(3)
	v_mov_b32_e32 v231, v216
	v_mov_b32_e32 v216, v215
	s_waitcnt lgkmcnt(1)
	v_mov_b32_e32 v233, v224
	v_mov_b32_e32 v224, v223
	v_pk_fma_f32 v[178:179], v[178:179], v[216:217], v[224:225]
	v_mov_b32_e32 v215, v220
	s_waitcnt lgkmcnt(0)
	v_mov_b32_e32 v217, v228
	v_pk_mul_f32 v[156:157], v[160:161], v[156:157] op_sel_hi:[0,1]
	v_mov_b32_e32 v220, v219
	v_mov_b32_e32 v228, v227
	v_pk_mul_f32 v[180:181], v[160:161], v[180:181] op_sel_hi:[0,1]
	v_mov_b32_e32 v230, v214
	v_mov_b32_e32 v232, v222
	v_pk_mul_f32 v[158:159], v[160:161], v[158:159] op_sel_hi:[0,1]
	v_mov_b32_e32 v214, v218
	v_mov_b32_e32 v216, v226
	v_pk_fma_f32 v[156:157], v[156:157], v[220:221], v[228:229]
	v_pk_fma_f32 v[180:181], v[180:181], v[230:231], v[232:233]
	v_pk_fma_f32 v[214:215], v[158:159], v[214:215], v[216:217]
	v_bfe_u32 v161, v179, 16, 1
	v_cvt_pk_bf16_f32 v164, v180, v178
	v_bfe_u32 v216, v181, 16, 1
	v_cvt_pk_bf16_f32 v159, v215, v157
	v_cvt_pk_bf16_f32 v158, v214, v156
	v_med3_f32 v180, v180, s55, v210
	v_med3_f32 v213, v178, s55, v210
	v_mov_b32_e32 v178, 0
	v_add3_u32 v161, v179, v161, s54
	v_add3_u32 v216, v181, v216, s54
	v_cvt_pk_fp8_f32 v178, v180, v213
	v_med3_f32 v180, v181, s55, v210
	v_med3_f32 v181, v179, s55, v210
	v_med3_f32 v213, v214, s55, v210
	v_med3_f32 v156, v156, s55, v210
	v_mov_b32_e32 v179, 0
	v_cvt_pk_fp8_f32 v179, v213, v156
	v_med3_f32 v156, v215, s55, v210
	v_med3_f32 v157, v157, s55, v210
	v_cvt_pk_fp8_f32 v178, v180, v181 op_sel:[0,0,1]
	v_cvt_pk_fp8_f32 v179, v156, v157 op_sel:[0,0,1]
	v_lshrrev_b32_e32 v216, 16, v216
	v_and_or_b32 v157, v161, s52, v216
	v_mov_b32_e32 v156, v164
	ds_write_b128 v203, v[156:159]
	global_store_dwordx2 v[150:151], v[178:179], off offset:1024
	ds_read_b128 v[156:159], v189 offset:6144
	ds_read_b128 v[178:181], v189 offset:6160
	ds_read_b128 v[214:217], v190 offset:6144
	ds_read_b128 v[218:221], v190 offset:6160
	v_pk_mul_f32 v[152:153], v[160:161], v[152:153] op_sel_hi:[0,1]
	s_waitcnt lgkmcnt(3)
	v_mov_b32_e32 v223, v158
	v_mov_b32_e32 v158, v157
	s_waitcnt lgkmcnt(1)
	v_mov_b32_e32 v225, v216
	v_mov_b32_e32 v216, v215
	v_pk_fma_f32 v[152:153], v[152:153], v[158:159], v[216:217]
	v_mov_b32_e32 v157, v180
	s_waitcnt lgkmcnt(0)
	v_mov_b32_e32 v159, v220
	v_pk_mul_f32 v[146:147], v[160:161], v[146:147] op_sel_hi:[0,1]
	v_mov_b32_e32 v180, v179
	v_mov_b32_e32 v220, v219
	v_pk_mul_f32 v[154:155], v[160:161], v[154:155] op_sel_hi:[0,1]
	v_mov_b32_e32 v222, v156
	v_mov_b32_e32 v224, v214
	v_pk_mul_f32 v[148:149], v[160:161], v[148:149] op_sel_hi:[0,1]
	v_mov_b32_e32 v156, v178
	v_mov_b32_e32 v158, v218
	v_pk_fma_f32 v[146:147], v[146:147], v[180:181], v[220:221]
	v_pk_fma_f32 v[154:155], v[154:155], v[222:223], v[224:225]
	v_pk_fma_f32 v[156:157], v[148:149], v[156:157], v[158:159]
	v_bfe_u32 v158, v153, 16, 1
	v_cvt_pk_bf16_f32 v159, v154, v152
	v_bfe_u32 v161, v155, 16, 1
	v_cvt_pk_bf16_f32 v149, v157, v147
	v_cvt_pk_bf16_f32 v148, v156, v146
	v_med3_f32 v154, v154, s55, v210
	v_med3_f32 v160, v152, s55, v210
	v_mov_b32_e32 v152, 0
	v_add3_u32 v158, v153, v158, s54
	v_add3_u32 v161, v155, v161, s54
	v_cvt_pk_fp8_f32 v152, v154, v160
	v_med3_f32 v154, v155, s55, v210
	v_med3_f32 v155, v153, s55, v210
	v_med3_f32 v156, v156, s55, v210
	v_med3_f32 v146, v146, s55, v210
	v_mov_b32_e32 v153, 0
	v_cvt_pk_fp8_f32 v153, v156, v146
	v_med3_f32 v146, v157, s55, v210
	v_med3_f32 v147, v147, s55, v210
	v_cvt_pk_fp8_f32 v152, v154, v155 op_sel:[0,0,1]
	v_cvt_pk_fp8_f32 v153, v146, v147 op_sel:[0,0,1]
	v_lshrrev_b32_e32 v161, 16, v161
	v_and_or_b32 v147, v158, s52, v161
	v_mov_b32_e32 v146, v159
	ds_write_b128 v204, v[146:149]
	global_store_dwordx2 v[150:151], v[152:153], off offset:1536
	global_load_dwordx4 v[146:149], v[168:169], off
	s_nop 0
	global_load_dwordx4 v[150:153], v[170:171], off
	global_load_dwordx4 v[154:157], v[172:173], off
	global_load_dwordx4 v[158:161], v[174:175], off
	s_cmp_lg_u32 s27, 48
	s_cbranch_scc0 .LBB0_1401
	s_add_i32 s22, s24, 16
	s_ashr_i32 s23, s22, 31
	s_lshl_b64 s[22:23], s[22:23], 12
	v_lshl_add_u64 v[126:127], v[166:167], 0, s[22:23]
	s_add_i32 s22, s24, 17
	s_ashr_i32 s23, s22, 31
	s_lshl_b64 s[22:23], s[22:23], 12
	v_lshl_add_u64 v[142:143], v[166:167], 0, s[22:23]
	global_load_dwordx4 v[114:117], v[126:127], off
	global_load_dwordx4 v[118:121], v[126:127], off offset:1024
	global_load_dwordx4 v[122:125], v[126:127], off offset:2048
	s_nop 0
	global_load_dwordx4 v[126:129], v[126:127], off offset:3072
	s_nop 0
	global_load_dwordx4 v[130:133], v[142:143], off
	global_load_dwordx4 v[134:137], v[142:143], off offset:1024
	global_load_dwordx4 v[138:141], v[142:143], off offset:2048
	s_nop 0
	global_load_dwordx4 v[142:145], v[142:143], off offset:3072
